# stack19 = stack16 + expert-phase preamble: prefix of tiles per class by DPP row_shr/row_bcast adds instead of 13 ds_bpermute round trips
# speedup vs baseline: 1.0057x; 1.0030x over previous
; DEVINL void phase5(const Params& P, unsigned char* smem) {
;     ...
;     if (t < 64) {
;         const int c0 = (int)ccnt[t * 64], c1 = t < 48 ? (int)ccnt[(64 + t) * 64] : 0;
;         const int n0 = (c0 + 79) / 80, n1 = (c1 + 79) / 80;
;         int i0 = n0, i1 = n1;
; #pragma unroll
;         for (int d = 1; d < 64; d <<= 1) { const int u0 = __shfl_up(i0, d), u1 = __shfl_up(i1, d); if (t >= d) { i0 += u0; i1 += u1; } }
;         const int tot0 = __shfl(i0, 63);
;         s_cv[t] = c0; s_cp[t] = i0 - n0;
;         if (t < 48) { s_cv[64 + t] = c1; s_cp[64 + t] = tot0 + i1 - n1; }
;         if (t == 47) s_cp[112] = tot0 + i1;
.LBB0_683:
	s_or_b64 exec, exec, s[4:5]
	s_waitcnt vmcnt(0)
	v_add_u32_e32 v2, 0x4f, v1
	s_mov_b32 s2, 0x66666667
	v_mul_hi_i32 v2, v2, s2
	v_lshrrev_b32_e32 v4, 31, v2
	v_ashrrev_i32_e32 v5, 5, v2
	v_add_u32_e32 v2, 0x4f, v3
	v_mul_hi_i32 v2, v2, s2
	v_lshrrev_b32_e32 v6, 31, v2
	v_ashrrev_i32_e32 v2, 5, v2
	v_add_u32_e32 v2, v2, v6
	v_add_u32_e32 v10, v5, v4
	v_mov_b32_e32 v4, v2
	v_mov_b32_e32 v7, v10
	s_nop 1
	v_add_u32_dpp v7, v7, v7 row_shr:1 row_mask:0xf bank_mask:0xf bound_ctrl:1
	v_add_u32_dpp v4, v4, v4 row_shr:1 row_mask:0xf bank_mask:0xf bound_ctrl:1
	s_nop 0
	v_add_u32_dpp v7, v7, v7 row_shr:2 row_mask:0xf bank_mask:0xf bound_ctrl:1
	v_add_u32_dpp v4, v4, v4 row_shr:2 row_mask:0xf bank_mask:0xf bound_ctrl:1
	s_nop 0
	v_add_u32_dpp v7, v7, v7 row_shr:4 row_mask:0xf bank_mask:0xf bound_ctrl:1
	v_add_u32_dpp v4, v4, v4 row_shr:4 row_mask:0xf bank_mask:0xf bound_ctrl:1
	s_nop 0
	v_add_u32_dpp v7, v7, v7 row_shr:8 row_mask:0xf bank_mask:0xf bound_ctrl:1
	v_add_u32_dpp v4, v4, v4 row_shr:8 row_mask:0xf bank_mask:0xf bound_ctrl:1
	s_nop 0
	v_add_u32_dpp v7, v7, v7 row_bcast:15 row_mask:0xa bank_mask:0xf
	v_add_u32_dpp v4, v4, v4 row_bcast:15 row_mask:0xa bank_mask:0xf
	s_nop 0
	v_add_u32_dpp v7, v7, v7 row_bcast:31 row_mask:0xc bank_mask:0xf
	v_add_u32_dpp v4, v4, v4 row_bcast:31 row_mask:0xc bank_mask:0xf
	s_nop 1
	v_readlane_b32 s2, v7, 63
	s_nop 1
	v_mov_b32_e32 v5, s2
	v_lshl_add_u32 v6, v0, 2, 0
	v_add_u32_e32 v8, 0x24200, v6
	ds_write_b32 v8, v1
	v_sub_u32_e32 v1, v7, v10
	v_add_u32_e32 v7, 0x24400, v6
	ds_write_b32 v7, v1
	s_and_saveexec_b64 s[4:5], s[6:7]
	s_cbranch_execz .LBB0_685
	v_add_u32_e32 v1, 0x24300, v6
	s_waitcnt lgkmcnt(2)
	v_sub_u32_e32 v2, v5, v2
	v_add_u32_e32 v2, v2, v4
	v_add_u32_e32 v6, 0x24500, v6
	ds_write_b32 v1, v3
	ds_write_b32 v6, v2
